# P8 bf16 GEMM: LDS image re-laid as 8-row x 128-B subtiles so each LDS-DMA instruction fetches full cache lines; k-half 1 fragment reads via second base
# speedup vs baseline: 1.0045x; 1.0045x over previous
.LBB0_491:
	v_lshl_or_b32 v2, s23, 8, v186
	v_ashrrev_i32_e32 v3, 31, v2
	v_lshl_add_u64 v[4:5], v[2:3], 2, s[30:31]
	global_load_dwordx4 v[10:13], v[4:5], off offset:16
	global_load_dwordx4 v[6:9], v[4:5], off
	global_load_dwordx4 v[182:185], v[4:5], off offset:528
	global_load_dwordx4 v[192:195], v[4:5], off offset:512
	s_lshl_b64 s[22:23], s[28:29], 12
	v_readlane_b32 s6, v254, 40
	v_lshl_add_u64 v[14:15], v[154:155], 0, v[2:3]
	v_lshl_add_u64 v[14:15], v[14:15], 2, s[26:27]
	global_load_dwordx4 v[206:209], v[14:15], off
	global_load_dwordx4 v[210:213], v[14:15], off offset:16
	global_load_dwordx4 v[214:217], v[14:15], off offset:512
	global_load_dwordx4 v[218:221], v[14:15], off offset:528
	s_add_u32 s22, s6, s22
	v_readlane_b32 s6, v254, 41
	v_lshl_add_u64 v[14:15], v[156:157], 0, v[2:3]
	v_lshl_add_u64 v[14:15], v[14:15], 2, s[26:27]
	global_load_dwordx4 v[222:225], v[14:15], off
	global_load_dwordx4 v[226:229], v[14:15], off offset:16
	global_load_dwordx4 v[230:233], v[14:15], off offset:512
	global_load_dwordx4 v[234:237], v[14:15], off offset:528
	s_addc_u32 s23, s6, s23
	s_mov_b64 s[28:29], s[20:21]
	v_lshl_add_u64 v[14:15], v[158:159], 0, v[2:3]
	v_lshl_add_u64 v[14:15], v[14:15], 2, s[26:27]
	global_load_dwordx4 v[238:241], v[14:15], off
	global_load_dwordx4 v[242:245], v[14:15], off offset:16
	global_load_dwordx4 v[196:199], v[14:15], off offset:512
	global_load_dwordx4 v[200:203], v[14:15], off offset:528
	s_waitcnt vmcnt(10)
	v_pk_mul_f32 v[10:11], v[10:11], s[12:13] op_sel_hi:[1,0]
	v_pk_mul_f32 v[4:5], v[8:9], s[12:13] op_sel_hi:[1,0]
	v_pk_mul_f32 v[6:7], v[6:7], s[12:13] op_sel_hi:[1,0]
	v_pk_mul_f32 v[8:9], v[12:13], s[12:13] op_sel_hi:[1,0]
	v_pk_mul_f32 v[12:13], v[194:195], s[12:13] op_sel_hi:[1,0]
	v_pk_mul_f32 v[14:15], v[192:193], s[12:13] op_sel_hi:[1,0]
	v_pk_mul_f32 v[16:17], v[184:185], s[12:13] op_sel_hi:[1,0]
	v_pk_mul_f32 v[178:179], v[182:183], s[12:13] op_sel_hi:[1,0]
	v_lshl_add_u64 v[180:181], v[154:155], 0, v[2:3]
	v_lshl_add_u64 v[180:181], v[180:181], 1, s[22:23]
	v_pk_fma_f32 v[142:143], v[142:143], v[6:7], v[206:207]
	v_pk_fma_f32 v[144:145], v[144:145], v[4:5], v[208:209]
	v_pk_fma_f32 v[138:139], v[138:139], v[10:11], v[210:211]
	v_pk_fma_f32 v[140:141], v[140:141], v[8:9], v[212:213]
	v_cvt_pk_bf16_f32 v142, v142, v143
	v_cvt_pk_bf16_f32 v143, v144, v145
	v_cvt_pk_bf16_f32 v144, v138, v139
	v_cvt_pk_bf16_f32 v145, v140, v141
	global_store_dwordx4 v[180:181], v[142:145], off
	s_waitcnt vmcnt(9)
	v_pk_fma_f32 v[134:135], v[134:135], v[14:15], v[214:215]
	v_pk_fma_f32 v[136:137], v[136:137], v[12:13], v[216:217]
	v_pk_fma_f32 v[130:131], v[130:131], v[178:179], v[218:219]
	v_pk_fma_f32 v[132:133], v[132:133], v[16:17], v[220:221]
	v_cvt_pk_bf16_f32 v134, v134, v135
	v_cvt_pk_bf16_f32 v135, v136, v137
	v_cvt_pk_bf16_f32 v136, v130, v131
	v_cvt_pk_bf16_f32 v137, v132, v133
	global_store_dwordx4 v[180:181], v[134:137], off offset:256
	v_lshl_add_u64 v[192:193], v[160:161], 0, v[2:3]
	v_lshl_add_u64 v[192:193], v[192:193], 2, s[26:27]
	global_load_dwordx4 v[138:141], v[192:193], off
	global_load_dwordx4 v[142:145], v[192:193], off offset:16
	global_load_dwordx4 v[130:133], v[192:193], off offset:512
	global_load_dwordx4 v[134:137], v[192:193], off offset:528
	s_waitcnt vmcnt(12)
	v_lshl_add_u64 v[180:181], v[156:157], 0, v[2:3]
	v_lshl_add_u64 v[180:181], v[180:181], 1, s[22:23]
	v_pk_fma_f32 v[126:127], v[126:127], v[6:7], v[222:223]
	v_pk_fma_f32 v[128:129], v[128:129], v[4:5], v[224:225]
	v_pk_fma_f32 v[122:123], v[122:123], v[10:11], v[226:227]
	v_pk_fma_f32 v[124:125], v[124:125], v[8:9], v[228:229]
	v_cvt_pk_bf16_f32 v126, v126, v127
	v_cvt_pk_bf16_f32 v127, v128, v129
	v_cvt_pk_bf16_f32 v128, v122, v123
	v_cvt_pk_bf16_f32 v129, v124, v125
	global_store_dwordx4 v[180:181], v[126:129], off
	s_waitcnt vmcnt(11)
	v_pk_fma_f32 v[118:119], v[118:119], v[14:15], v[230:231]
	v_pk_fma_f32 v[120:121], v[120:121], v[12:13], v[232:233]
	v_pk_fma_f32 v[114:115], v[114:115], v[178:179], v[234:235]
	v_pk_fma_f32 v[116:117], v[116:117], v[16:17], v[236:237]
	v_cvt_pk_bf16_f32 v118, v118, v119
	v_cvt_pk_bf16_f32 v119, v120, v121
	v_cvt_pk_bf16_f32 v120, v114, v115
	v_cvt_pk_bf16_f32 v121, v116, v117
	global_store_dwordx4 v[180:181], v[118:121], off offset:256
	v_lshl_add_u64 v[192:193], v[162:163], 0, v[2:3]
	v_lshl_add_u64 v[192:193], v[192:193], 2, s[26:27]
	global_load_dwordx4 v[122:125], v[192:193], off
	global_load_dwordx4 v[126:129], v[192:193], off offset:16
	global_load_dwordx4 v[114:117], v[192:193], off offset:512
	global_load_dwordx4 v[118:121], v[192:193], off offset:528
	s_waitcnt vmcnt(14)
	v_lshl_add_u64 v[180:181], v[158:159], 0, v[2:3]
	v_lshl_add_u64 v[180:181], v[180:181], 1, s[22:23]
	v_pk_fma_f32 v[110:111], v[110:111], v[6:7], v[238:239]
	v_pk_fma_f32 v[112:113], v[112:113], v[4:5], v[240:241]
	v_pk_fma_f32 v[106:107], v[106:107], v[10:11], v[242:243]
	v_pk_fma_f32 v[108:109], v[108:109], v[8:9], v[244:245]
	v_cvt_pk_bf16_f32 v110, v110, v111
	v_cvt_pk_bf16_f32 v111, v112, v113
	v_cvt_pk_bf16_f32 v112, v106, v107
	v_cvt_pk_bf16_f32 v113, v108, v109
	global_store_dwordx4 v[180:181], v[110:113], off
	s_waitcnt vmcnt(13)
	v_pk_fma_f32 v[102:103], v[102:103], v[14:15], v[196:197]
	v_pk_fma_f32 v[104:105], v[104:105], v[12:13], v[198:199]
	v_pk_fma_f32 v[98:99], v[98:99], v[178:179], v[200:201]
	v_pk_fma_f32 v[100:101], v[100:101], v[16:17], v[202:203]
	v_cvt_pk_bf16_f32 v102, v102, v103
	v_cvt_pk_bf16_f32 v103, v104, v105
	v_cvt_pk_bf16_f32 v104, v98, v99
	v_cvt_pk_bf16_f32 v105, v100, v101
	global_store_dwordx4 v[180:181], v[102:105], off offset:256
	v_lshl_add_u64 v[192:193], v[164:165], 0, v[2:3]
	v_lshl_add_u64 v[192:193], v[192:193], 2, s[26:27]
	global_load_dwordx4 v[106:109], v[192:193], off
	global_load_dwordx4 v[110:113], v[192:193], off offset:16
	global_load_dwordx4 v[98:101], v[192:193], off offset:512
	global_load_dwordx4 v[102:105], v[192:193], off offset:528
	s_waitcnt vmcnt(14)
	v_lshl_add_u64 v[180:181], v[160:161], 0, v[2:3]
	v_lshl_add_u64 v[180:181], v[180:181], 1, s[22:23]
	v_pk_fma_f32 v[94:95], v[94:95], v[6:7], v[138:139]
	v_pk_fma_f32 v[96:97], v[96:97], v[4:5], v[140:141]
	v_pk_fma_f32 v[90:91], v[90:91], v[10:11], v[142:143]
	v_pk_fma_f32 v[92:93], v[92:93], v[8:9], v[144:145]
	v_cvt_pk_bf16_f32 v94, v94, v95
	v_cvt_pk_bf16_f32 v95, v96, v97
	v_cvt_pk_bf16_f32 v96, v90, v91
	v_cvt_pk_bf16_f32 v97, v92, v93
	global_store_dwordx4 v[180:181], v[94:97], off
	s_waitcnt vmcnt(13)
	v_pk_fma_f32 v[86:87], v[86:87], v[14:15], v[130:131]
	v_pk_fma_f32 v[88:89], v[88:89], v[12:13], v[132:133]
	v_pk_fma_f32 v[82:83], v[82:83], v[178:179], v[134:135]
	v_pk_fma_f32 v[84:85], v[84:85], v[16:17], v[136:137]
	v_cvt_pk_bf16_f32 v86, v86, v87
	v_cvt_pk_bf16_f32 v87, v88, v89
	v_cvt_pk_bf16_f32 v88, v82, v83
	v_cvt_pk_bf16_f32 v89, v84, v85
	global_store_dwordx4 v[180:181], v[86:89], off offset:256
	v_lshl_add_u64 v[200:201], v[166:167], 0, v[2:3]
	v_lshl_add_u64 v[200:201], v[200:201], 2, s[26:27]
	global_load_dwordx4 v[90:93], v[200:201], off
	global_load_dwordx4 v[94:97], v[200:201], off offset:16
	global_load_dwordx4 v[82:85], v[200:201], off offset:512
	global_load_dwordx4 v[86:89], v[200:201], off offset:528
	s_waitcnt vmcnt(14)
	v_lshl_add_u64 v[180:181], v[162:163], 0, v[2:3]
	v_lshl_add_u64 v[180:181], v[180:181], 1, s[22:23]
	v_pk_fma_f32 v[78:79], v[78:79], v[6:7], v[122:123]
	v_pk_fma_f32 v[80:81], v[80:81], v[4:5], v[124:125]
	v_pk_fma_f32 v[74:75], v[74:75], v[10:11], v[126:127]
	v_pk_fma_f32 v[76:77], v[76:77], v[8:9], v[128:129]
	v_cvt_pk_bf16_f32 v78, v78, v79
	v_cvt_pk_bf16_f32 v79, v80, v81
	v_cvt_pk_bf16_f32 v80, v74, v75
	v_cvt_pk_bf16_f32 v81, v76, v77
	global_store_dwordx4 v[180:181], v[78:81], off
	s_waitcnt vmcnt(13)
	v_pk_fma_f32 v[70:71], v[70:71], v[14:15], v[114:115]
	v_pk_fma_f32 v[72:73], v[72:73], v[12:13], v[116:117]
	v_pk_fma_f32 v[66:67], v[66:67], v[178:179], v[118:119]
	v_pk_fma_f32 v[68:69], v[68:69], v[16:17], v[120:121]
	v_cvt_pk_bf16_f32 v70, v70, v71
	v_cvt_pk_bf16_f32 v71, v72, v73
	v_cvt_pk_bf16_f32 v72, v66, v67
	v_cvt_pk_bf16_f32 v73, v68, v69
	global_store_dwordx4 v[180:181], v[70:73], off offset:256
	v_lshl_add_u64 v[200:201], v[168:169], 0, v[2:3]
	v_lshl_add_u64 v[200:201], v[200:201], 2, s[26:27]
	global_load_dwordx4 v[74:77], v[200:201], off
	global_load_dwordx4 v[78:81], v[200:201], off offset:16
	global_load_dwordx4 v[66:69], v[200:201], off offset:512
	global_load_dwordx4 v[70:73], v[200:201], off offset:528
	s_waitcnt vmcnt(14)
	v_lshl_add_u64 v[180:181], v[164:165], 0, v[2:3]
	v_lshl_add_u64 v[180:181], v[180:181], 1, s[22:23]
	v_pk_fma_f32 v[62:63], v[62:63], v[6:7], v[106:107]
	v_pk_fma_f32 v[64:65], v[64:65], v[4:5], v[108:109]
	v_pk_fma_f32 v[58:59], v[58:59], v[10:11], v[110:111]
	v_pk_fma_f32 v[60:61], v[60:61], v[8:9], v[112:113]
	v_cvt_pk_bf16_f32 v62, v62, v63
	v_cvt_pk_bf16_f32 v63, v64, v65
	v_cvt_pk_bf16_f32 v64, v58, v59
	v_cvt_pk_bf16_f32 v65, v60, v61
	global_store_dwordx4 v[180:181], v[62:65], off
	s_waitcnt vmcnt(13)
	v_pk_fma_f32 v[54:55], v[54:55], v[14:15], v[98:99]
	v_pk_fma_f32 v[56:57], v[56:57], v[12:13], v[100:101]
	v_pk_fma_f32 v[50:51], v[50:51], v[178:179], v[102:103]
	v_pk_fma_f32 v[52:53], v[52:53], v[16:17], v[104:105]
	v_cvt_pk_bf16_f32 v54, v54, v55
	v_cvt_pk_bf16_f32 v55, v56, v57
	v_cvt_pk_bf16_f32 v56, v50, v51
	v_cvt_pk_bf16_f32 v57, v52, v53
	global_store_dwordx4 v[180:181], v[54:57], off offset:256
	s_waitcnt vmcnt(10)
	v_lshl_add_u64 v[180:181], v[166:167], 0, v[2:3]
	v_lshl_add_u64 v[180:181], v[180:181], 1, s[22:23]
	v_pk_fma_f32 v[46:47], v[46:47], v[6:7], v[90:91]
	v_pk_fma_f32 v[48:49], v[48:49], v[4:5], v[92:93]
	v_pk_fma_f32 v[42:43], v[42:43], v[10:11], v[94:95]
	v_pk_fma_f32 v[44:45], v[44:45], v[8:9], v[96:97]
	v_cvt_pk_bf16_f32 v46, v46, v47
	v_cvt_pk_bf16_f32 v47, v48, v49
	v_cvt_pk_bf16_f32 v48, v42, v43
	v_cvt_pk_bf16_f32 v49, v44, v45
	global_store_dwordx4 v[180:181], v[46:49], off
	s_waitcnt vmcnt(9)
	v_pk_fma_f32 v[38:39], v[38:39], v[14:15], v[82:83]
	v_pk_fma_f32 v[40:41], v[40:41], v[12:13], v[84:85]
	v_pk_fma_f32 v[34:35], v[34:35], v[178:179], v[86:87]
	v_pk_fma_f32 v[36:37], v[36:37], v[16:17], v[88:89]
	v_cvt_pk_bf16_f32 v38, v38, v39
	v_cvt_pk_bf16_f32 v39, v40, v41
	v_cvt_pk_bf16_f32 v40, v34, v35
	v_cvt_pk_bf16_f32 v41, v36, v37
	global_store_dwordx4 v[180:181], v[38:41], off offset:256
	s_waitcnt vmcnt(6)
	v_lshl_add_u64 v[180:181], v[168:169], 0, v[2:3]
	v_lshl_add_u64 v[180:181], v[180:181], 1, s[22:23]
	s_mov_b32 s23, s14
	s_mov_b32 s22, s16
	v_pk_fma_f32 v[30:31], v[30:31], v[6:7], v[74:75]
	v_pk_fma_f32 v[32:33], v[32:33], v[4:5], v[76:77]
	v_pk_fma_f32 v[26:27], v[26:27], v[10:11], v[78:79]
	v_pk_fma_f32 v[28:29], v[28:29], v[8:9], v[80:81]
	v_cvt_pk_bf16_f32 v30, v30, v31
	v_cvt_pk_bf16_f32 v31, v32, v33
	v_cvt_pk_bf16_f32 v32, v26, v27
	v_cvt_pk_bf16_f32 v33, v28, v29
	global_store_dwordx4 v[180:181], v[30:33], off
	s_waitcnt vmcnt(5)
	v_pk_fma_f32 v[22:23], v[22:23], v[14:15], v[66:67]
	v_pk_fma_f32 v[24:25], v[24:25], v[12:13], v[68:69]
	v_pk_fma_f32 v[18:19], v[18:19], v[178:179], v[70:71]
	v_pk_fma_f32 v[20:21], v[20:21], v[16:17], v[72:73]
	v_cvt_pk_bf16_f32 v22, v22, v23
	v_cvt_pk_bf16_f32 v23, v24, v25
	v_cvt_pk_bf16_f32 v24, v18, v19
	v_cvt_pk_bf16_f32 v25, v20, v21
	global_store_dwordx4 v[180:181], v[22:25], off offset:256
	s_mov_b64 s[26:27], s[18:19]
	s_and_b64 vcc, exec, s[0:1]
	s_cbranch_vccnz .LBB0_500

.LBB0_612:
	s_cmp_lt_i32 s94, 9
	s_cselect_b64 s[4:5], -1, 0
	s_and_b64 s[0:1], s[4:5], s[0:1]
	s_andn2_b64 vcc, exec, s[0:1]
	s_cbranch_vccnz .LBB0_625
	v_readlane_b32 s0, v254, 38
	s_cmpk_gt_i32 s0, 0x47f
	v_readfirstlane_b32 s2, v0
	v_readlane_b32 s1, v254, 39
	s_cbranch_scc1 .LBB0_625
	v_lshrrev_b32_e32 v1, 5, v0
	s_waitcnt vmcnt(0)
	v_lshrrev_b32_e32 v3, 1, v0
	v_and_b32_e32 v1, 4, v1
	v_bfe_u32 v2, v0, 2, 2
	v_and_b32_e32 v13, 24, v3
	v_or3_b32 v1, v1, v2, v13
	v_lshlrev_b32_e32 v2, 4, v0
	v_or_b32_e32 v10, 0x2000, v2
	s_add_u32 s33, s82, 0x4300000
	v_lshrrev_b32_e32 v3, 7, v10
	s_movk_i32 s0, 0x60
	v_readlane_b32 s6, v254, 38
	s_addc_u32 s36, s83, 0
	v_and_or_b32 v4, v3, s0, v1
	v_bfe_u32 v14, v0, 2, 4
	s_movk_i32 s0, 0x70
	s_ashr_i32 s38, s6, 31
	v_and_or_b32 v3, v3, s0, v14
	s_lshr_b32 s0, s38, 29
	s_add_i32 s0, s6, s0
	s_lshr_b32 s8, s2, 6
	s_mov_b32 s10, s6
	s_ashr_i32 s6, s0, 3
	s_and_b32 s0, s0, -8
	s_lshr_b32 s1, s2, 8
	s_lshl_b32 s37, s8, 10
	s_sub_i32 s0, s10, s0
	v_readlane_b32 s7, v254, 39
	s_cmp_lt_i32 s0, 0
	s_movk_i32 s39, 0x91
	s_cselect_b32 s7, s39, 0x90
	s_mul_i32 s0, s0, s7
	s_add_i32 s0, s0, s6
	s_ashr_i32 s6, s0, 31
	s_lshr_b32 s6, s6, 26
	s_add_i32 s6, s0, s6
	s_ashr_i32 s7, s6, 6
	s_andn2_b32 s6, s6, 63
	s_sub_i32 s6, s0, s6
	s_bfe_i32 s0, s6, 0x80000
	s_bfe_u32 s0, s0, 0x3000c
	s_add_i32 s9, s6, s0
	s_bfe_i32 s0, s9, 0x80000
	s_and_b32 s9, s9, 0xf8
	s_sub_i32 s6, s6, s9
	s_lshl_b32 s7, s7, 3
	s_sext_i32_i16 s0, s0
	s_sext_i32_i8 s6, s6
	v_and_b32_e32 v5, 32, v0
	s_lshr_b32 s0, s0, 3
	s_add_i32 s16, s7, s6
	v_bitop3_b32 v11, v2, v5, 48 bitop3:0x6c
	v_and_b32_e32 v12, 64, v0
	s_ashr_i32 s17, s16, 31
	s_bfe_i64 s[10:11], s[0:1], 0x100000
	v_or_b32_e32 v2, v11, v12
	s_lshl_b64 s[6:7], s[16:17], 20
	s_lshl_b64 s[10:11], s[10:11], 20
	v_lshl_or_b32 v132, v3, 12, v2
	v_lshrrev_b32_e32 v3, 3, v0
	s_add_u32 s30, s33, s10
	v_and_or_b32 v1, v3, 32, v1
	s_addc_u32 s31, s36, s11
	s_add_i32 s17, s37, 0
	v_lshl_or_b32 v134, v1, 12, v2
	s_add_i32 m0, s17, 0x10000
	v_readlane_b32 s9, v254, 36
	v_lshrrev_b32_e32 v226, 3, v204
	v_and_b32_e32 v227, 7, v204
	v_xor_b32_e32 v227, v227, v226
	v_lshlrev_b32_e32 v227, 4, v227
	v_mov_b32_e32 v229, s89
	v_lshl_add_u32 v228, v229, 3, v226
	v_lshl_or_b32 v136, v228, 12, v227
	v_add_u32_e32 v132, 0x40000, v136
	v_and_b32_e32 v230, 1, v229
	v_lshlrev_b32_e32 v230, 4, v230
	v_bfe_u32 v231, v229, 1, 1
	v_lshlrev_b32_e32 v231, 2, v231
	v_lshrrev_b32_e32 v232, 2, v229
	v_lshlrev_b32_e32 v232, 5, v232
	v_bfe_u32 v233, v226, 2, 1
	v_lshlrev_b32_e32 v233, 3, v233
	v_and_b32_e32 v234, 3, v226
	v_add3_u32 v230, v230, v231, v232
	v_add3_u32 v230, v230, v233, v234
	v_lshl_or_b32 v134, v230, 12, v227
	v_add_u32_e32 v130, 0x40000, v134
	global_load_lds_dwordx4 v134, s[30:31]
	s_add_i32 m0, s17, 0x12000
	s_nop 0
	v_and_or_b32 v1, v3, 48, v14
	s_add_u32 s28, s9, s6
	v_readlane_b32 s6, v254, 37
	s_nop 0
	global_load_lds_dwordx4 v130, s[30:31]
	s_addc_u32 s29, s6, s7
	s_mov_b32 m0, s17
	s_add_i32 s40, s17, 0x2000
	global_load_lds_dwordx4 v136, s[28:29]
	s_mov_b32 m0, s40
	s_add_u32 s6, s30, 0x80000
	global_load_lds_dwordx4 v132, s[28:29]
	s_addc_u32 s7, s31, 0
	s_add_i32 m0, s17, 0x14000
	v_mov_b32_e32 v135, 0
	global_load_lds_dwordx4 v134, s[6:7]
	s_add_i32 m0, s17, 0x16000
	v_mov_b32_e32 v131, v135
	global_load_lds_dwordx4 v130, s[6:7]
	s_add_u32 s6, s28, 0x80000
	s_addc_u32 s7, s29, 0
	s_add_i32 s41, s17, 0x4000
	s_mov_b32 m0, s41
	s_add_i32 s42, s17, 0x6000
	global_load_lds_dwordx4 v136, s[6:7]
	s_mov_b32 m0, s42
	v_mov_b32_e32 v137, v135
	global_load_lds_dwordx4 v132, s[6:7]
	v_mov_b32_e32 v133, v135
	s_mov_b32 s43, 0
	v_lshl_add_u64 v[8:9], s[30:31], 0, v[134:135]
	v_lshl_add_u64 v[6:7], s[30:31], 0, v[130:131]
	v_lshl_add_u64 v[4:5], s[28:29], 0, v[136:137]
	v_lshl_add_u64 v[2:3], s[28:29], 0, v[132:133]
	s_cmp_lg_u32 s1, 1
	s_mov_b64 s[6:7], 0x80000
	s_cbranch_scc1 .LBB0_616
	s_barrier
.LBB0_616:
	s_lshl_b32 s8, s8, 5
	s_and_b32 s13, s8, 0x60
	s_mov_b64 s[8:9], 0x80
	s_add_i32 m0, s17, 0x18000
	v_lshl_add_u64 v[8:9], v[8:9], 0, s[8:9]
	s_lshl_b32 s12, s1, 13
	s_lshl_b32 s14, s13, 7
	s_waitcnt vmcnt(4)
	s_barrier
	global_load_lds_dwordx4 v[8:9], off
	v_lshl_add_u64 v[6:7], v[6:7], 0, s[8:9]
	s_add_i32 m0, s17, 0x1a000
	s_add_i32 s44, s17, 0x8000
	s_add_i32 s45, s17, 0xa000
	global_load_lds_dwordx4 v[6:7], off
	v_lshl_add_u64 v[4:5], v[4:5], 0, s[8:9]
	s_mov_b32 m0, s44
	s_add_u32 s10, s30, 0x80080
	global_load_lds_dwordx4 v[4:5], off
	v_lshl_add_u64 v[2:3], v[2:3], 0, s[8:9]
	s_mov_b32 m0, s45
	s_addc_u32 s11, s31, 0
	global_load_lds_dwordx4 v[2:3], off
	s_add_i32 m0, s17, 0x1c000
	v_lshl_add_u64 v[2:3], s[10:11], 0, v[134:135]
	global_load_lds_dwordx4 v[2:3], off
	v_lshl_add_u64 v[2:3], s[10:11], 0, v[130:131]
	s_add_i32 m0, s17, 0x1e000
	s_sext_i32_i8 s53, s0
	global_load_lds_dwordx4 v[2:3], off
	v_and_b32_e32 v2, 15, v0
	v_lshlrev_b32_e32 v3, 1, v13
	v_lshlrev_b32_e32 v4, 2, v0
	v_lshlrev_b32_e32 v5, 6, v0
	s_movk_i32 s0, 0x3c0
	v_lshl_or_b32 v1, s1, 6, v2
	v_lshl_or_b32 v2, v2, 6, v3
	v_and_b32_e32 v4, 32, v4
	v_and_or_b32 v3, v5, s0, v3
	v_bitop3_b32 v146, s14, v3, v4 bitop3:0xf6
	v_lshlrev_b32_e32 v3, 9, v0
	v_bitop3_b32 v2, v2, s12, v4 bitop3:0xde
	v_and_b32_e32 v3, 0x30000, v3
	v_lshlrev_b32_e32 v4, 12, v14
	v_or3_b32 v3, v11, v3, v4
	v_mov_b32_e32 v138, v136
	v_lshlrev_b32_e32 v3, 5, v10
	s_waitcnt vmcnt(6)
	v_and_b32_e32 v3, 0x70000, v3
	v_or3_b32 v3, v11, v3, v4
	s_add_i32 s47, 0, 0x10000
	s_add_i32 s48, 0, 0x14000
	s_ashr_i32 s46, s92, 31
	v_or_b32_e32 v147, s13, v13
	v_mov_b32_e32 v139, v135
	v_mov_b32_e32 v140, v132
	v_mov_b32_e32 v141, v135
	v_mov_b64_e32 v[142:143], 0x480
	v_mov_b64_e32 v[144:145], 0x47f
	v_add_u32_e32 v148, s47, v146
	v_add_u32_e32 v149, 0, v2
	v_add_u32_e32 v150, s48, v146
	v_and_b32_e32 v226, 15, v204
	v_lshrrev_b32_e32 v227, 4, v204
	v_and_b32_e32 v228, 7, v226
	v_xor_b32_e32 v227, v227, v228
	v_lshlrev_b32_e32 v227, 4, v227
	v_lshl_or_b32 v227, v228, 7, v227
	v_lshrrev_b32_e32 v228, 3, v226
	v_lshl_or_b32 v227, v228, 10, v227
	v_add_u32_e32 v149, s12, v227
	v_add_u32_e32 v146, s14, v227
	v_add_u32_e32 v148, s47, v146
	v_add_u32_e32 v150, s48, v146
	v_xor_b32_e32 v229, 64, v149
	v_xor_b32_e32 v230, 64, v148
	v_xor_b32_e32 v231, 64, v150
	s_mov_b32 s49, 0x80000
	s_mov_b64 s[10:11], 0x90000
	s_mov_b32 s50, 0x90000
	s_mov_b64 s[12:13], 0xa0000
	s_mov_b32 s51, 0xa0000
	s_mov_b64 s[14:15], 0xb0000
	s_mov_b32 s52, 0xb0000
	s_barrier

.LBB0_620:
	ds_read_b128 v[152:155], v148
	ds_read_b128 v[156:159], v230
	ds_read_b128 v[160:163], v148 offset:2048
	ds_read_b128 v[164:167], v230 offset:2048
	s_add_u32 s30, s28, 0xfff80080
	s_addc_u32 s31, s29, -1
	s_cmp_eq_u32 s60, 28
	s_cselect_b32 s35, s21, s31
	s_cselect_b32 s34, s54, s30
	s_cselect_b32 s31, s19, s57
	s_cselect_b32 s30, s55, s56
	v_lshl_add_u64 v[200:201], s[28:29], 0, v[138:139]
	s_add_i32 m0, s17, 0xc000
	ds_read_b128 v[168:171], v149
	ds_read_b128 v[172:175], v229
	ds_read_b128 v[176:179], v149 offset:2048
	ds_read_b128 v[180:183], v229 offset:2048
	ds_read_b128 v[184:187], v149 offset:4096
	ds_read_b128 v[188:191], v229 offset:4096
	ds_read_b128 v[192:195], v149 offset:6144
	ds_read_b128 v[196:199], v229 offset:6144
	global_load_lds_dwordx4 v[200:201], off
	v_lshl_add_u64 v[200:201], s[28:29], 0, v[140:141]
	s_add_i32 m0, s17, 0xe000
	s_nop 0
	global_load_lds_dwordx4 v[200:201], off
	s_waitcnt lgkmcnt(8)
	s_barrier
	s_waitcnt lgkmcnt(0)
	s_setprio 1
	s_waitcnt lgkmcnt(0)
	v_mfma_f32_16x16x32_bf16 v[126:129], v[152:155], v[168:171], v[126:129]
	v_mfma_f32_16x16x32_bf16 v[122:125], v[160:163], v[168:171], v[122:125]
	v_mfma_f32_16x16x32_bf16 v[118:121], v[152:155], v[176:179], v[118:121]
	v_mfma_f32_16x16x32_bf16 v[114:117], v[160:163], v[176:179], v[114:117]
	v_mfma_f32_16x16x32_bf16 v[102:105], v[152:155], v[184:187], v[102:105]
	v_mfma_f32_16x16x32_bf16 v[98:101], v[160:163], v[184:187], v[98:101]
	v_mfma_f32_16x16x32_bf16 v[86:89], v[152:155], v[192:195], v[86:89]
	v_mfma_f32_16x16x32_bf16 v[82:85], v[160:163], v[192:195], v[82:85]
	v_mfma_f32_16x16x32_bf16 v[126:129], v[156:159], v[172:175], v[126:129]
	v_mfma_f32_16x16x32_bf16 v[122:125], v[164:167], v[172:175], v[122:125]
	v_mfma_f32_16x16x32_bf16 v[118:121], v[156:159], v[180:183], v[118:121]
	v_mfma_f32_16x16x32_bf16 v[114:117], v[164:167], v[180:183], v[114:117]
	v_mfma_f32_16x16x32_bf16 v[102:105], v[156:159], v[188:191], v[102:105]
	v_mfma_f32_16x16x32_bf16 v[98:101], v[164:167], v[188:191], v[98:101]
	v_mfma_f32_16x16x32_bf16 v[86:89], v[156:159], v[196:199], v[86:89]
	v_mfma_f32_16x16x32_bf16 v[82:85], v[164:167], v[196:199], v[82:85]
	s_setprio 0
	s_barrier
	s_add_i32 s61, s47, s37
	v_lshl_add_u64 v[218:219], s[30:31], 0, v[134:135]
	s_mov_b32 m0, s61
	ds_read_b128 v[200:203], v150
	ds_read_b128 v[206:209], v231
	ds_read_b128 v[210:213], v150 offset:2048
	ds_read_b128 v[214:217], v231 offset:2048
	global_load_lds_dwordx4 v[218:219], off
	v_lshl_add_u64 v[220:221], s[30:31], 0, v[130:131]
	s_add_i32 m0, s61, 0x2000
	s_nop 0
	global_load_lds_dwordx4 v[220:221], off
	s_barrier
	s_waitcnt lgkmcnt(0)
	s_setprio 1
	s_waitcnt lgkmcnt(0)
	v_mfma_f32_16x16x32_bf16 v[110:113], v[200:203], v[168:171], v[110:113]
	v_mfma_f32_16x16x32_bf16 v[106:109], v[210:213], v[168:171], v[106:109]
	v_mfma_f32_16x16x32_bf16 v[94:97], v[200:203], v[176:179], v[94:97]
	v_mfma_f32_16x16x32_bf16 v[90:93], v[210:213], v[176:179], v[90:93]
	v_mfma_f32_16x16x32_bf16 v[78:81], v[200:203], v[184:187], v[78:81]
	v_mfma_f32_16x16x32_bf16 v[74:77], v[210:213], v[184:187], v[74:77]
	v_mfma_f32_16x16x32_bf16 v[70:73], v[200:203], v[192:195], v[70:73]
	v_mfma_f32_16x16x32_bf16 v[66:69], v[210:213], v[192:195], v[66:69]
	v_mfma_f32_16x16x32_bf16 v[110:113], v[206:209], v[172:175], v[110:113]
	v_mfma_f32_16x16x32_bf16 v[106:109], v[214:217], v[172:175], v[106:109]
	v_mfma_f32_16x16x32_bf16 v[94:97], v[206:209], v[180:183], v[94:97]
	v_mfma_f32_16x16x32_bf16 v[90:93], v[214:217], v[180:183], v[90:93]
	v_mfma_f32_16x16x32_bf16 v[78:81], v[206:209], v[188:191], v[78:81]
	v_mfma_f32_16x16x32_bf16 v[74:77], v[214:217], v[188:191], v[74:77]
	v_mfma_f32_16x16x32_bf16 v[70:73], v[206:209], v[196:199], v[70:73]
	v_mfma_f32_16x16x32_bf16 v[66:69], v[214:217], v[196:199], v[66:69]
	s_setprio 0
	s_mov_b32 m0, s17
	v_lshl_add_u64 v[222:223], s[34:35], 0, v[136:137]
	s_barrier
	ds_read_b128 v[168:171], v149 offset:16384
	ds_read_b128 v[172:175], v229 offset:16384
	ds_read_b128 v[176:179], v149 offset:18432
	ds_read_b128 v[180:183], v229 offset:18432
	ds_read_b128 v[184:187], v149 offset:20480
	ds_read_b128 v[188:191], v229 offset:20480
	ds_read_b128 v[192:195], v149 offset:22528
	ds_read_b128 v[196:199], v229 offset:22528
	global_load_lds_dwordx4 v[222:223], off
	v_lshl_add_u64 v[224:225], s[34:35], 0, v[132:133]
	s_mov_b32 m0, s40
	s_nop 0
	global_load_lds_dwordx4 v[224:225], off
	s_barrier
	s_waitcnt lgkmcnt(0)
	s_setprio 1
	s_waitcnt lgkmcnt(0)
	v_mfma_f32_16x16x32_bf16 v[62:65], v[152:155], v[168:171], v[62:65]
	v_mfma_f32_16x16x32_bf16 v[58:61], v[160:163], v[168:171], v[58:61]
	v_mfma_f32_16x16x32_bf16 v[54:57], v[152:155], v[176:179], v[54:57]
	v_mfma_f32_16x16x32_bf16 v[50:53], v[160:163], v[176:179], v[50:53]
	v_mfma_f32_16x16x32_bf16 v[38:41], v[152:155], v[184:187], v[38:41]
	v_mfma_f32_16x16x32_bf16 v[34:37], v[160:163], v[184:187], v[34:37]
	v_mfma_f32_16x16x32_bf16 v[22:25], v[152:155], v[192:195], v[22:25]
	v_mfma_f32_16x16x32_bf16 v[18:21], v[160:163], v[192:195], v[18:21]
	v_mfma_f32_16x16x32_bf16 v[62:65], v[156:159], v[172:175], v[62:65]
	v_mfma_f32_16x16x32_bf16 v[58:61], v[164:167], v[172:175], v[58:61]
	v_mfma_f32_16x16x32_bf16 v[54:57], v[156:159], v[180:183], v[54:57]
	v_mfma_f32_16x16x32_bf16 v[50:53], v[164:167], v[180:183], v[50:53]
	v_mfma_f32_16x16x32_bf16 v[38:41], v[156:159], v[188:191], v[38:41]
	v_mfma_f32_16x16x32_bf16 v[34:37], v[164:167], v[188:191], v[34:37]
	v_mfma_f32_16x16x32_bf16 v[22:25], v[156:159], v[196:199], v[22:25]
	v_mfma_f32_16x16x32_bf16 v[18:21], v[164:167], v[196:199], v[18:21]
	s_setprio 0
	s_barrier
	s_add_u32 s62, s30, 0x80000
	s_addc_u32 s63, s31, 0
	s_add_i32 s61, s48, s37
	v_lshl_add_u64 v[152:153], s[62:63], 0, v[134:135]
	s_mov_b32 m0, s61
	s_nop 0
	global_load_lds_dwordx4 v[152:153], off
	v_lshl_add_u64 v[152:153], s[62:63], 0, v[130:131]
	s_add_i32 m0, s61, 0x2000
	s_nop 0
	global_load_lds_dwordx4 v[152:153], off
	s_waitcnt vmcnt(6)
	s_barrier
	s_setprio 1
	v_mfma_f32_16x16x32_bf16 v[46:49], v[200:203], v[168:171], v[46:49]
	v_mfma_f32_16x16x32_bf16 v[42:45], v[210:213], v[168:171], v[42:45]
	v_mfma_f32_16x16x32_bf16 v[30:33], v[200:203], v[176:179], v[30:33]
	v_mfma_f32_16x16x32_bf16 v[26:29], v[210:213], v[176:179], v[26:29]
	v_mfma_f32_16x16x32_bf16 v[14:17], v[200:203], v[184:187], v[14:17]
	v_mfma_f32_16x16x32_bf16 v[10:13], v[210:213], v[184:187], v[10:13]
	v_mfma_f32_16x16x32_bf16 v[6:9], v[200:203], v[192:195], v[6:9]
	v_mfma_f32_16x16x32_bf16 v[2:5], v[210:213], v[192:195], v[2:5]
	v_mfma_f32_16x16x32_bf16 v[46:49], v[206:209], v[172:175], v[46:49]
	v_mfma_f32_16x16x32_bf16 v[42:45], v[214:217], v[172:175], v[42:45]
	v_mfma_f32_16x16x32_bf16 v[30:33], v[206:209], v[180:183], v[30:33]
	v_mfma_f32_16x16x32_bf16 v[26:29], v[214:217], v[180:183], v[26:29]
	v_mfma_f32_16x16x32_bf16 v[14:17], v[206:209], v[188:191], v[14:17]
	v_mfma_f32_16x16x32_bf16 v[10:13], v[214:217], v[188:191], v[10:13]
	v_mfma_f32_16x16x32_bf16 v[6:9], v[206:209], v[196:199], v[6:9]
	v_mfma_f32_16x16x32_bf16 v[2:5], v[214:217], v[196:199], v[2:5]
	s_setprio 0
	s_add_i32 s61, 0, 0x18000
	v_add_u32_e32 v151, s61, v146
	v_xor_b32_e32 v232, 64, v151
	s_barrier
	ds_read_b128 v[152:155], v151
	ds_read_b128 v[156:159], v232
	ds_read_b128 v[160:163], v151 offset:2048
	ds_read_b128 v[164:167], v232 offset:2048
	s_add_u32 s34, s34, 0x80000
	s_addc_u32 s35, s35, 0
	s_mov_b32 m0, s41
	v_lshl_add_u64 v[200:201], s[34:35], 0, v[136:137]
	ds_read_b128 v[168:171], v149 offset:32768
	ds_read_b128 v[172:175], v229 offset:32768
	ds_read_b128 v[176:179], v149 offset:34816
	ds_read_b128 v[180:183], v229 offset:34816
	ds_read_b128 v[184:187], v149 offset:36864
	ds_read_b128 v[188:191], v229 offset:36864
	ds_read_b128 v[192:195], v149 offset:38912
	ds_read_b128 v[196:199], v229 offset:38912
	global_load_lds_dwordx4 v[200:201], off
	v_lshl_add_u64 v[200:201], s[34:35], 0, v[132:133]
	s_mov_b32 m0, s42
	s_nop 0
	global_load_lds_dwordx4 v[200:201], off
	s_waitcnt lgkmcnt(8)
	s_barrier
	s_waitcnt lgkmcnt(0)
	s_setprio 1
	s_waitcnt lgkmcnt(0)
	v_mfma_f32_16x16x32_bf16 v[126:129], v[152:155], v[168:171], v[126:129]
	v_mfma_f32_16x16x32_bf16 v[122:125], v[160:163], v[168:171], v[122:125]
	v_mfma_f32_16x16x32_bf16 v[118:121], v[152:155], v[176:179], v[118:121]
	v_mfma_f32_16x16x32_bf16 v[114:117], v[160:163], v[176:179], v[114:117]
	v_mfma_f32_16x16x32_bf16 v[102:105], v[152:155], v[184:187], v[102:105]
	v_mfma_f32_16x16x32_bf16 v[98:101], v[160:163], v[184:187], v[98:101]
	v_mfma_f32_16x16x32_bf16 v[86:89], v[152:155], v[192:195], v[86:89]
	v_mfma_f32_16x16x32_bf16 v[82:85], v[160:163], v[192:195], v[82:85]
	v_mfma_f32_16x16x32_bf16 v[126:129], v[156:159], v[172:175], v[126:129]
	v_mfma_f32_16x16x32_bf16 v[122:125], v[164:167], v[172:175], v[122:125]
	v_mfma_f32_16x16x32_bf16 v[118:121], v[156:159], v[180:183], v[118:121]
	v_mfma_f32_16x16x32_bf16 v[114:117], v[164:167], v[180:183], v[114:117]
	v_mfma_f32_16x16x32_bf16 v[102:105], v[156:159], v[188:191], v[102:105]
	v_mfma_f32_16x16x32_bf16 v[98:101], v[164:167], v[188:191], v[98:101]
	v_mfma_f32_16x16x32_bf16 v[86:89], v[156:159], v[196:199], v[86:89]
	v_mfma_f32_16x16x32_bf16 v[82:85], v[164:167], v[196:199], v[82:85]
	s_setprio 0
	s_barrier
	s_add_i32 s34, 0, 0x1c000
	s_add_i32 s35, s61, s37
	v_add_u32_e32 v151, s34, v146
	v_xor_b32_e32 v232, 64, v151
	v_lshl_add_u64 v[218:219], v[218:219], 0, s[8:9]
	s_mov_b32 m0, s35
	ds_read_b128 v[200:203], v151
	ds_read_b128 v[206:209], v232
	ds_read_b128 v[210:213], v151 offset:2048
	ds_read_b128 v[214:217], v232 offset:2048
	global_load_lds_dwordx4 v[218:219], off
	v_lshl_add_u64 v[218:219], v[220:221], 0, s[8:9]
	s_add_i32 m0, s35, 0x2000
	s_nop 0
	global_load_lds_dwordx4 v[218:219], off
	s_barrier
	s_waitcnt lgkmcnt(0)
	s_setprio 1
	s_waitcnt lgkmcnt(0)
	v_mfma_f32_16x16x32_bf16 v[110:113], v[200:203], v[168:171], v[110:113]
	v_mfma_f32_16x16x32_bf16 v[106:109], v[210:213], v[168:171], v[106:109]
	v_mfma_f32_16x16x32_bf16 v[94:97], v[200:203], v[176:179], v[94:97]
	v_mfma_f32_16x16x32_bf16 v[90:93], v[210:213], v[176:179], v[90:93]
	v_mfma_f32_16x16x32_bf16 v[78:81], v[200:203], v[184:187], v[78:81]
	v_mfma_f32_16x16x32_bf16 v[74:77], v[210:213], v[184:187], v[74:77]
	v_mfma_f32_16x16x32_bf16 v[70:73], v[200:203], v[192:195], v[70:73]
	v_mfma_f32_16x16x32_bf16 v[66:69], v[210:213], v[192:195], v[66:69]
	v_mfma_f32_16x16x32_bf16 v[110:113], v[206:209], v[172:175], v[110:113]
	v_mfma_f32_16x16x32_bf16 v[106:109], v[214:217], v[172:175], v[106:109]
	v_mfma_f32_16x16x32_bf16 v[94:97], v[206:209], v[180:183], v[94:97]
	v_mfma_f32_16x16x32_bf16 v[90:93], v[214:217], v[180:183], v[90:93]
	v_mfma_f32_16x16x32_bf16 v[78:81], v[206:209], v[188:191], v[78:81]
	v_mfma_f32_16x16x32_bf16 v[74:77], v[214:217], v[188:191], v[74:77]
	v_mfma_f32_16x16x32_bf16 v[70:73], v[206:209], v[196:199], v[70:73]
	v_mfma_f32_16x16x32_bf16 v[66:69], v[214:217], v[196:199], v[66:69]
	s_setprio 0
	s_mov_b32 m0, s44
	v_lshl_add_u64 v[218:219], v[222:223], 0, s[8:9]
	s_barrier
	ds_read_b128 v[168:171], v149 offset:49152
	ds_read_b128 v[172:175], v229 offset:49152
	ds_read_b128 v[176:179], v149 offset:51200
	ds_read_b128 v[180:183], v229 offset:51200
	ds_read_b128 v[184:187], v149 offset:53248
	ds_read_b128 v[188:191], v229 offset:53248
	ds_read_b128 v[192:195], v149 offset:55296
	ds_read_b128 v[196:199], v229 offset:55296
	global_load_lds_dwordx4 v[218:219], off
	v_lshl_add_u64 v[218:219], v[224:225], 0, s[8:9]
	s_mov_b32 m0, s45
	s_nop 0
	global_load_lds_dwordx4 v[218:219], off
	s_barrier
	s_waitcnt lgkmcnt(0)
	s_setprio 1
	s_waitcnt lgkmcnt(0)
	v_mfma_f32_16x16x32_bf16 v[62:65], v[152:155], v[168:171], v[62:65]
	v_mfma_f32_16x16x32_bf16 v[58:61], v[160:163], v[168:171], v[58:61]
	v_mfma_f32_16x16x32_bf16 v[54:57], v[152:155], v[176:179], v[54:57]
	v_mfma_f32_16x16x32_bf16 v[50:53], v[160:163], v[176:179], v[50:53]
	v_mfma_f32_16x16x32_bf16 v[38:41], v[152:155], v[184:187], v[38:41]
	v_mfma_f32_16x16x32_bf16 v[34:37], v[160:163], v[184:187], v[34:37]
	v_mfma_f32_16x16x32_bf16 v[22:25], v[152:155], v[192:195], v[22:25]
	v_mfma_f32_16x16x32_bf16 v[18:21], v[160:163], v[192:195], v[18:21]
	v_mfma_f32_16x16x32_bf16 v[62:65], v[156:159], v[172:175], v[62:65]
	v_mfma_f32_16x16x32_bf16 v[58:61], v[164:167], v[172:175], v[58:61]
	v_mfma_f32_16x16x32_bf16 v[54:57], v[156:159], v[180:183], v[54:57]
	v_mfma_f32_16x16x32_bf16 v[50:53], v[164:167], v[180:183], v[50:53]
	v_mfma_f32_16x16x32_bf16 v[38:41], v[156:159], v[188:191], v[38:41]
	v_mfma_f32_16x16x32_bf16 v[34:37], v[164:167], v[188:191], v[34:37]
	v_mfma_f32_16x16x32_bf16 v[22:25], v[156:159], v[196:199], v[22:25]
	v_mfma_f32_16x16x32_bf16 v[18:21], v[164:167], v[196:199], v[18:21]
	s_setprio 0
	s_barrier
	s_add_u32 s30, s30, 0x80080
	s_addc_u32 s31, s31, 0
	s_add_i32 s34, s34, s37
	v_lshl_add_u64 v[152:153], s[30:31], 0, v[134:135]
	s_mov_b32 m0, s34
	s_nop 0
	global_load_lds_dwordx4 v[152:153], off
	v_lshl_add_u64 v[152:153], s[30:31], 0, v[130:131]
	s_add_i32 m0, s34, 0x2000
	s_nop 0
	global_load_lds_dwordx4 v[152:153], off
	s_waitcnt vmcnt(6)
	s_barrier
	s_setprio 1
	v_mfma_f32_16x16x32_bf16 v[46:49], v[200:203], v[168:171], v[46:49]
	v_mfma_f32_16x16x32_bf16 v[42:45], v[210:213], v[168:171], v[42:45]
	v_mfma_f32_16x16x32_bf16 v[30:33], v[200:203], v[176:179], v[30:33]
	v_mfma_f32_16x16x32_bf16 v[26:29], v[210:213], v[176:179], v[26:29]
	v_mfma_f32_16x16x32_bf16 v[14:17], v[200:203], v[184:187], v[14:17]
	v_mfma_f32_16x16x32_bf16 v[10:13], v[210:213], v[184:187], v[10:13]
	v_mfma_f32_16x16x32_bf16 v[6:9], v[200:203], v[192:195], v[6:9]
	v_mfma_f32_16x16x32_bf16 v[2:5], v[210:213], v[192:195], v[2:5]
	v_mfma_f32_16x16x32_bf16 v[46:49], v[206:209], v[172:175], v[46:49]
	v_mfma_f32_16x16x32_bf16 v[42:45], v[214:217], v[172:175], v[42:45]
	v_mfma_f32_16x16x32_bf16 v[30:33], v[206:209], v[180:183], v[30:33]
	v_mfma_f32_16x16x32_bf16 v[26:29], v[214:217], v[180:183], v[26:29]
	v_mfma_f32_16x16x32_bf16 v[14:17], v[206:209], v[188:191], v[14:17]
	v_mfma_f32_16x16x32_bf16 v[10:13], v[214:217], v[188:191], v[10:13]
	v_mfma_f32_16x16x32_bf16 v[6:9], v[206:209], v[196:199], v[6:9]
	v_mfma_f32_16x16x32_bf16 v[2:5], v[214:217], v[196:199], v[2:5]
	s_setprio 0
	s_add_i32 s60, s60, 2
	s_add_u32 s28, s28, 0x100
	s_addc_u32 s29, s29, 0
	s_add_u32 s56, s56, 0x100
	s_addc_u32 s57, s57, 0
	s_cmp_gt_u32 s60, 29
	s_barrier
	s_cbranch_scc0 .LBB0_620
	v_lshl_add_u32 v152, s16, 8, v1
	v_lshl_or_b32 v154, s53, 8, v147
	v_ashrrev_i32_e32 v153, 31, v152
	v_ashrrev_i32_e32 v155, 31, v154
	v_lshlrev_b64 v[156:157], 12, v[152:153]
	v_lshl_add_u64 v[156:157], s[96:97], 0, v[156:157]
	v_lshlrev_b64 v[154:155], 1, v[154:155]
	v_lshl_add_u64 v[156:157], v[156:157], 0, v[154:155]
	v_cvt_pk_bf16_f32 v62, v62, v63
	v_cvt_pk_bf16_f32 v63, v64, v65
	v_cvt_pk_bf16_f32 v64, v58, v59
	v_add_co_u32_e32 v58, vcc, s49, v156
	v_cvt_pk_bf16_f32 v70, v70, v71
	v_cvt_pk_bf16_f32 v71, v72, v73
	v_cvt_pk_bf16_f32 v72, v66, v67
	v_lshl_add_u64 v[66:67], v[156:157], 0, s[6:7]
	v_addc_co_u32_e32 v59, vcc, 0, v157, vcc
	v_cvt_pk_bf16_f32 v46, v46, v47
	v_cvt_pk_bf16_f32 v47, v48, v49
	v_cvt_pk_bf16_f32 v48, v42, v43
	v_cvt_pk_bf16_f32 v49, v44, v45
	v_cvt_pk_bf16_f32 v110, v110, v111
	v_cvt_pk_bf16_f32 v111, v112, v113
	v_cvt_pk_bf16_f32 v112, v106, v107
	v_or_b32_e32 v106, 16, v152
	global_store_dwordx4 v[66:67], v[46:49], off offset:256
	v_ashrrev_i32_e32 v107, 31, v106
	v_cvt_pk_bf16_f32 v94, v94, v95
	v_add_co_u32_e32 v48, vcc, s50, v156
	v_cvt_pk_bf16_f32 v95, v96, v97
	v_cvt_pk_bf16_f32 v96, v90, v91
	v_or_b32_e32 v90, 32, v152
	v_lshl_add_u64 v[46:47], v[156:157], 0, s[10:11]
	v_addc_co_u32_e32 v49, vcc, 0, v157, vcc
	v_cvt_pk_bf16_f32 v30, v30, v31
	v_cvt_pk_bf16_f32 v31, v32, v33
	v_cvt_pk_bf16_f32 v32, v26, v27
	v_cvt_pk_bf16_f32 v33, v28, v29
	v_lshlrev_b64 v[106:107], 12, v[106:107]
	v_ashrrev_i32_e32 v91, 31, v90
	v_cvt_pk_bf16_f32 v78, v78, v79
	v_cvt_pk_bf16_f32 v79, v80, v81
	v_cvt_pk_bf16_f32 v80, v74, v75
	v_or_b32_e32 v74, 48, v152
	global_store_dwordx4 v[46:47], v[30:33], off offset:256
	v_cvt_pk_bf16_f32 v113, v108, v109
	v_lshl_add_u64 v[106:107], s[96:97], 0, v[106:107]
	v_add_co_u32_e32 v32, vcc, s51, v156
	v_lshlrev_b64 v[90:91], 12, v[90:91]
	v_ashrrev_i32_e32 v75, 31, v74
	v_lshl_add_u64 v[30:31], v[156:157], 0, s[12:13]
	v_addc_co_u32_e32 v33, vcc, 0, v157, vcc
	v_cvt_pk_bf16_f32 v14, v14, v15
	v_cvt_pk_bf16_f32 v15, v16, v17
	v_cvt_pk_bf16_f32 v16, v10, v11
	v_cvt_pk_bf16_f32 v17, v12, v13
	global_store_dwordx4 v[156:157], v[110:113], off offset:256
	v_cvt_pk_bf16_f32 v97, v92, v93
	v_lshl_add_u64 v[90:91], s[96:97], 0, v[90:91]
	v_lshl_add_u64 v[110:111], v[106:107], 0, v[154:155]
	v_lshlrev_b64 v[74:75], 12, v[74:75]
	global_store_dwordx4 v[30:31], v[14:17], off offset:256
	global_store_dwordx4 v[110:111], v[94:97], off offset:256
	v_cvt_pk_bf16_f32 v81, v76, v77
	v_add_co_u32_e32 v16, vcc, s52, v156
	v_lshl_add_u64 v[94:95], v[90:91], 0, v[154:155]
	v_lshl_add_u64 v[74:75], s[96:97], 0, v[74:75]
	v_addc_co_u32_e32 v17, vcc, 0, v157, vcc
	v_cvt_pk_bf16_f32 v126, v126, v127
	v_cvt_pk_bf16_f32 v127, v128, v129
	v_cvt_pk_bf16_f32 v128, v122, v123
	v_cvt_pk_bf16_f32 v129, v124, v125
	v_cvt_pk_bf16_f32 v106, v118, v119
	v_cvt_pk_bf16_f32 v107, v120, v121
	v_cvt_pk_bf16_f32 v108, v114, v115
	v_cvt_pk_bf16_f32 v109, v116, v117
	v_cvt_pk_bf16_f32 v90, v102, v103
	v_cvt_pk_bf16_f32 v91, v104, v105
	v_cvt_pk_bf16_f32 v92, v98, v99
	v_cvt_pk_bf16_f32 v93, v100, v101
	global_store_dwordx4 v[94:95], v[78:81], off offset:256
	v_cvt_pk_bf16_f32 v76, v82, v83
	v_cvt_pk_bf16_f32 v77, v84, v85
	v_lshl_add_u64 v[78:79], v[74:75], 0, v[154:155]
	v_cvt_pk_bf16_f32 v74, v86, v87
	v_cvt_pk_bf16_f32 v75, v88, v89
	v_cvt_pk_bf16_f32 v73, v68, v69
	v_cvt_pk_bf16_f32 v65, v60, v61
	v_cvt_pk_bf16_f32 v42, v54, v55
	v_cvt_pk_bf16_f32 v43, v56, v57
	v_cvt_pk_bf16_f32 v44, v50, v51
	v_cvt_pk_bf16_f32 v45, v52, v53
	v_cvt_pk_bf16_f32 v26, v38, v39
	v_cvt_pk_bf16_f32 v27, v40, v41
	v_cvt_pk_bf16_f32 v28, v34, v35
	v_cvt_pk_bf16_f32 v29, v36, v37
	v_lshl_add_u64 v[14:15], v[156:157], 0, s[14:15]
	v_cvt_pk_bf16_f32 v10, v22, v23
	v_cvt_pk_bf16_f32 v11, v24, v25
	v_cvt_pk_bf16_f32 v12, v18, v19
	v_cvt_pk_bf16_f32 v13, v20, v21
	v_cvt_pk_bf16_f32 v6, v6, v7
	v_cvt_pk_bf16_f32 v7, v8, v9
	v_cvt_pk_bf16_f32 v8, v2, v3
	v_cvt_pk_bf16_f32 v9, v4, v5
	s_and_b64 vcc, exec, s[0:1]
	s_mov_b32 s53, s18
	s_mov_b32 s16, s20
	s_mov_b64 s[30:31], s[26:27]
	s_mov_b64 s[28:29], s[22:23]
	global_store_dwordx4 v[156:157], v[126:129], off
	global_store_dwordx4 v[110:111], v[106:109], off
	global_store_dwordx4 v[94:95], v[90:93], off
	global_store_dwordx4 v[78:79], v[74:77], off
	global_store_dwordx4 v[78:79], v[70:73], off offset:256
	global_store_dwordx4 v[58:59], v[62:65], off
	global_store_dwordx4 v[48:49], v[42:45], off
	global_store_dwordx4 v[32:33], v[26:29], off
	global_store_dwordx4 v[16:17], v[10:13], off
	global_store_dwordx4 v[14:15], v[6:9], off offset:256
	s_cbranch_vccz .LBB0_617
	s_waitcnt vmcnt(0)
	s_cmpk_gt_u32 s2, 0xff
	s_cbranch_scc1 .LBB0_624
	s_barrier

.LBB0_752:
	s_waitcnt lgkmcnt(0)
	v_add_f32_e32 v34, v34, v35
	v_fmamk_f32 v34, v34, 0x3a000000, v107
	v_rsq_f32_e32 v48, v34
	v_lshl_add_u64 v[36:37], s[82:83], 0, v[100:101]
	v_add_co_u32_e32 v36, vcc, s39, v36
	s_nop 1
	v_addc_co_u32_e32 v37, vcc, 0, v37, vcc
	v_mul_f32_e32 v2, v48, v2
	v_mul_f32_e32 v3, v48, v3
	v_mul_f32_e32 v4, v48, v4
	v_mul_f32_e32 v5, v48, v5
	v_mul_f32_e32 v6, v48, v6
	v_mul_f32_e32 v7, v48, v7
	v_mul_f32_e32 v8, v48, v8
	v_mul_f32_e32 v9, v48, v9
	v_mul_f32_e32 v10, v48, v10
	v_mul_f32_e32 v11, v48, v11
	v_mul_f32_e32 v12, v48, v12
	v_mul_f32_e32 v13, v48, v13
	v_mul_f32_e32 v14, v48, v14
	v_mul_f32_e32 v15, v48, v15
	v_mul_f32_e32 v16, v48, v16
	v_mul_f32_e32 v17, v48, v17
	v_mul_f32_e32 v18, v48, v18
	v_mul_f32_e32 v19, v48, v19
	v_mul_f32_e32 v20, v48, v20
	v_mul_f32_e32 v21, v48, v21
	v_mul_f32_e32 v22, v48, v22
	v_mul_f32_e32 v23, v48, v23
	v_mul_f32_e32 v24, v48, v24
	v_mul_f32_e32 v25, v48, v25
	v_mul_f32_e32 v26, v48, v26
	v_mul_f32_e32 v27, v48, v27
	v_mul_f32_e32 v28, v48, v28
	v_mul_f32_e32 v29, v48, v29
	v_mul_f32_e32 v30, v48, v30
	v_mul_f32_e32 v31, v48, v31
	v_mul_f32_e32 v32, v48, v32
	v_mul_f32_e32 v33, v48, v33
	s_waitcnt vmcnt(9)
	v_mul_f32_e32 v2, v2, v128
	v_mul_f32_e32 v3, v3, v129
	v_mul_f32_e32 v32, v32, v130
	v_mul_f32_e32 v33, v33, v131
	v_add_f32_e32 v132, 1.0, v132
	v_add_f32_e32 v133, 1.0, v133
	v_add_f32_e32 v134, 1.0, v134
	v_add_f32_e32 v135, 1.0, v135
	v_fma_f32 v2, v2, v132, v136
	v_fma_f32 v3, v3, v133, v137
	v_fma_f32 v32, v32, v134, v138
	v_fma_f32 v33, v33, v135, v139
	v_mul_f32_e32 v2, 0x41800000, v2
	v_mul_f32_e32 v3, 0x41800000, v3
	v_mul_f32_e32 v32, 0x41800000, v32
	v_mul_f32_e32 v33, 0x41800000, v33
	v_med3_f32 v2, v2, s38, v122
	v_med3_f32 v3, v3, s38, v122
	v_med3_f32 v32, v32, s38, v122
	v_med3_f32 v33, v33, s38, v122
	v_cvt_pk_fp8_f32 v38, v2, v3
	global_load_dwordx4 v[128:131], v[76:77], off
	global_load_dwordx4 v[132:135], v118, s[34:35]
	global_load_dwordx4 v[136:139], v118, s[30:31]
	v_cvt_pk_fp8_f32 v38, v32, v33 op_sel:[0,0,1]
	global_store_dword v[36:37], v38, off
	s_waitcnt vmcnt(10)
	v_mul_f32_e32 v28, v28, v140
	v_mul_f32_e32 v29, v29, v141
	v_mul_f32_e32 v30, v30, v142
	v_mul_f32_e32 v31, v31, v143
	v_add_f32_e32 v144, 1.0, v144
	v_add_f32_e32 v145, 1.0, v145
	v_add_f32_e32 v146, 1.0, v146
	v_add_f32_e32 v147, 1.0, v147
	v_fma_f32 v28, v28, v144, v148
	v_fma_f32 v29, v29, v145, v149
	v_fma_f32 v30, v30, v146, v150
	v_fma_f32 v31, v31, v147, v151
	v_mul_f32_e32 v28, 0x41800000, v28
	v_mul_f32_e32 v29, 0x41800000, v29
	v_mul_f32_e32 v30, 0x41800000, v30
	v_mul_f32_e32 v31, 0x41800000, v31
	v_med3_f32 v28, v28, s38, v122
	v_med3_f32 v29, v29, s38, v122
	v_med3_f32 v30, v30, s38, v122
	v_med3_f32 v31, v31, s38, v122
	v_cvt_pk_fp8_f32 v39, v28, v29
	global_load_dwordx4 v[140:143], v[78:79], off
	global_load_dwordx4 v[144:147], v119, s[34:35]
	global_load_dwordx4 v[148:151], v119, s[30:31]
	v_cvt_pk_fp8_f32 v39, v30, v31 op_sel:[0,0,1]
	global_store_dword v[36:37], v39, off offset:256
	s_waitcnt vmcnt(11)
	v_mul_f32_e32 v24, v24, v152
	v_mul_f32_e32 v25, v25, v153
	v_mul_f32_e32 v26, v26, v154
	v_mul_f32_e32 v27, v27, v155
	v_add_f32_e32 v156, 1.0, v156
	v_add_f32_e32 v157, 1.0, v157
	v_add_f32_e32 v158, 1.0, v158
	v_add_f32_e32 v159, 1.0, v159
	v_fma_f32 v24, v24, v156, v160
	v_fma_f32 v25, v25, v157, v161
	v_fma_f32 v26, v26, v158, v162
	v_fma_f32 v27, v27, v159, v163
	v_mul_f32_e32 v24, 0x41800000, v24
	v_mul_f32_e32 v25, 0x41800000, v25
	v_mul_f32_e32 v26, 0x41800000, v26
	v_mul_f32_e32 v27, 0x41800000, v27
	v_med3_f32 v24, v24, s38, v122
	v_med3_f32 v25, v25, s38, v122
	v_med3_f32 v26, v26, s38, v122
	v_med3_f32 v27, v27, s38, v122
	v_cvt_pk_fp8_f32 v40, v24, v25
	global_load_dwordx4 v[152:155], v[80:81], off
	global_load_dwordx4 v[156:159], v120, s[34:35]
	global_load_dwordx4 v[160:163], v120, s[30:31]
	v_cvt_pk_fp8_f32 v40, v26, v27 op_sel:[0,0,1]
	global_store_dword v[36:37], v40, off offset:512
	s_waitcnt vmcnt(12)
	v_mul_f32_e32 v20, v20, v164
	v_mul_f32_e32 v21, v21, v165
	v_mul_f32_e32 v22, v22, v166
	v_mul_f32_e32 v23, v23, v167
	v_add_f32_e32 v168, 1.0, v168
	v_add_f32_e32 v169, 1.0, v169
	v_add_f32_e32 v170, 1.0, v170
	v_add_f32_e32 v171, 1.0, v171
	v_fma_f32 v20, v20, v168, v172
	v_fma_f32 v21, v21, v169, v173
	v_fma_f32 v22, v22, v170, v174
	v_fma_f32 v23, v23, v171, v175
	v_mul_f32_e32 v20, 0x41800000, v20
	v_mul_f32_e32 v21, 0x41800000, v21
	v_mul_f32_e32 v22, 0x41800000, v22
	v_mul_f32_e32 v23, 0x41800000, v23
	v_med3_f32 v20, v20, s38, v122
	v_med3_f32 v21, v21, s38, v122
	v_med3_f32 v22, v22, s38, v122
	v_med3_f32 v23, v23, s38, v122
	v_cvt_pk_fp8_f32 v41, v20, v21
	global_load_dwordx4 v[164:167], v[82:83], off
	global_load_dwordx4 v[168:171], v121, s[34:35]
	global_load_dwordx4 v[172:175], v121, s[30:31]
	v_cvt_pk_fp8_f32 v41, v22, v23 op_sel:[0,0,1]
	global_store_dword v[36:37], v41, off offset:768
	s_waitcnt vmcnt(12)
	v_mul_f32_e32 v16, v16, v128
	v_mul_f32_e32 v17, v17, v129
	v_mul_f32_e32 v18, v18, v130
	v_mul_f32_e32 v19, v19, v131
	v_add_f32_e32 v132, 1.0, v132
	v_add_f32_e32 v133, 1.0, v133
	v_add_f32_e32 v134, 1.0, v134
	v_add_f32_e32 v135, 1.0, v135
	v_fma_f32 v16, v16, v132, v136
	v_fma_f32 v17, v17, v133, v137
	v_fma_f32 v18, v18, v134, v138
	v_fma_f32 v19, v19, v135, v139
	v_mul_f32_e32 v16, 0x41800000, v16
	v_mul_f32_e32 v17, 0x41800000, v17
	v_mul_f32_e32 v18, 0x41800000, v18
	v_mul_f32_e32 v19, 0x41800000, v19
	v_med3_f32 v16, v16, s38, v122
	v_med3_f32 v17, v17, s38, v122
	v_med3_f32 v18, v18, s38, v122
	v_med3_f32 v19, v19, s38, v122
	v_cvt_pk_fp8_f32 v42, v16, v17
	s_nop 0
	v_cvt_pk_fp8_f32 v42, v18, v19 op_sel:[0,0,1]
	global_store_dword v[36:37], v42, off offset:1024
	s_waitcnt vmcnt(9)
	v_mul_f32_e32 v12, v12, v140
	v_mul_f32_e32 v13, v13, v141
	v_mul_f32_e32 v14, v14, v142
	v_mul_f32_e32 v15, v15, v143
	v_add_f32_e32 v144, 1.0, v144
	v_add_f32_e32 v145, 1.0, v145
	v_add_f32_e32 v146, 1.0, v146
	v_add_f32_e32 v147, 1.0, v147
	v_fma_f32 v12, v12, v144, v148
	v_fma_f32 v13, v13, v145, v149
	v_fma_f32 v14, v14, v146, v150
	v_fma_f32 v15, v15, v147, v151
	v_mul_f32_e32 v12, 0x41800000, v12
	v_mul_f32_e32 v13, 0x41800000, v13
	v_mul_f32_e32 v14, 0x41800000, v14
	v_mul_f32_e32 v15, 0x41800000, v15
	v_med3_f32 v12, v12, s38, v122
	v_med3_f32 v13, v13, s38, v122
	v_med3_f32 v14, v14, s38, v122
	v_med3_f32 v15, v15, s38, v122
	v_cvt_pk_fp8_f32 v43, v12, v13
	s_nop 0
	v_cvt_pk_fp8_f32 v43, v14, v15 op_sel:[0,0,1]
	global_store_dword v[36:37], v43, off offset:1280
	s_waitcnt vmcnt(6)
	v_mul_f32_e32 v8, v8, v152
	v_mul_f32_e32 v9, v9, v153
	v_mul_f32_e32 v10, v10, v154
	v_mul_f32_e32 v11, v11, v155
	v_add_f32_e32 v156, 1.0, v156
	v_add_f32_e32 v157, 1.0, v157
	v_add_f32_e32 v158, 1.0, v158
	v_add_f32_e32 v159, 1.0, v159
	v_fma_f32 v8, v8, v156, v160
	v_fma_f32 v9, v9, v157, v161
	v_fma_f32 v10, v10, v158, v162
	v_fma_f32 v11, v11, v159, v163
	v_mul_f32_e32 v8, 0x41800000, v8
	v_mul_f32_e32 v9, 0x41800000, v9
	v_mul_f32_e32 v10, 0x41800000, v10
	v_mul_f32_e32 v11, 0x41800000, v11
	v_med3_f32 v8, v8, s38, v122
	v_med3_f32 v9, v9, s38, v122
	v_med3_f32 v10, v10, s38, v122
	v_med3_f32 v11, v11, s38, v122
	v_cvt_pk_fp8_f32 v44, v8, v9
	s_nop 0
	v_cvt_pk_fp8_f32 v44, v10, v11 op_sel:[0,0,1]
	global_store_dword v[36:37], v44, off offset:1536
	s_waitcnt vmcnt(3)
	v_mul_f32_e32 v7, v7, v164
	v_mul_f32_e32 v6, v6, v165
	v_mul_f32_e32 v5, v5, v166
	v_mul_f32_e32 v4, v4, v167
	v_add_f32_e32 v168, 1.0, v168
	v_add_f32_e32 v169, 1.0, v169
	v_add_f32_e32 v170, 1.0, v170
	v_add_f32_e32 v171, 1.0, v171
	v_fma_f32 v7, v7, v168, v172
	v_fma_f32 v6, v6, v169, v173
	v_fma_f32 v5, v5, v170, v174
	v_fma_f32 v4, v4, v171, v175
	v_mul_f32_e32 v7, 0x41800000, v7
	v_mul_f32_e32 v6, 0x41800000, v6
	v_mul_f32_e32 v5, 0x41800000, v5
	v_mul_f32_e32 v4, 0x41800000, v4
	v_med3_f32 v7, v7, s38, v122
	v_med3_f32 v6, v6, s38, v122
	v_med3_f32 v5, v5, s38, v122
	v_med3_f32 v4, v4, s38, v122
	v_cvt_pk_fp8_f32 v45, v7, v6
	s_nop 0
	v_cvt_pk_fp8_f32 v45, v5, v4 op_sel:[0,0,1]
	global_store_dword v[36:37], v45, off offset:1792

.LBB0_1222:
	v_lshl_or_b32 v2, s47, 8, v187
	v_readlane_b32 s6, v254, 40
	v_ashrrev_i32_e32 v3, 31, v2
	v_readlane_b32 s15, v254, 41
	v_lshl_add_u64 v[12:13], v[2:3], 2, s[30:31]
	s_add_u32 s22, s6, s28
	s_addc_u32 s23, s15, s29
	s_add_u32 s24, s6, s24
	s_addc_u32 s25, s15, s25
	global_load_dwordx4 v[4:7], v[12:13], off offset:16
	global_load_dwordx4 v[8:11], v[12:13], off
	global_load_dwordx4 v[194:197], v[12:13], off offset:528
	global_load_dwordx4 v[198:201], v[12:13], off offset:512
	s_mov_b32 s47, s14
	s_mov_b64 s[26:27], s[20:21]
	v_lshl_add_u64 v[180:181], v[154:155], 0, v[2:3]
	v_lshl_add_u64 v[180:181], v[180:181], 1, s[22:23]
	global_load_dwordx4 v[214:217], v[180:181], off
	global_load_dwordx4 v[218:221], v[180:181], off offset:256
	v_lshl_add_u64 v[180:181], v[156:157], 0, v[2:3]
	v_lshl_add_u64 v[180:181], v[180:181], 1, s[22:23]
	global_load_dwordx4 v[222:225], v[180:181], off
	global_load_dwordx4 v[226:229], v[180:181], off offset:256
	v_lshl_add_u64 v[180:181], v[158:159], 0, v[2:3]
	v_lshl_add_u64 v[180:181], v[180:181], 1, s[22:23]
	global_load_dwordx4 v[230:233], v[180:181], off
	global_load_dwordx4 v[234:237], v[180:181], off offset:256
	v_lshl_add_u64 v[180:181], v[160:161], 0, v[2:3]
	v_lshl_add_u64 v[180:181], v[180:181], 1, s[22:23]
	global_load_dwordx4 v[238:241], v[180:181], off
	global_load_dwordx4 v[242:245], v[180:181], off offset:256
	v_lshl_add_u64 v[180:181], v[162:163], 0, v[2:3]
	v_lshl_add_u64 v[180:181], v[180:181], 1, s[22:23]
	global_load_dwordx4 v[246:249], v[180:181], off
	global_load_dwordx4 v[250:253], v[180:181], off offset:256
	s_waitcnt vmcnt(9)
	v_pk_mul_f32 v[16:17], v[6:7], s[12:13] op_sel_hi:[1,0]
	v_pk_mul_f32 v[12:13], v[10:11], s[12:13] op_sel_hi:[1,0]
	v_pk_mul_f32 v[14:15], v[8:9], s[12:13] op_sel_hi:[1,0]
	v_pk_mul_f32 v[178:179], v[4:5], s[12:13] op_sel_hi:[1,0]
	v_pk_mul_f32 v[8:9], v[196:197], s[12:13] op_sel_hi:[1,0]
	v_pk_mul_f32 v[4:5], v[200:201], s[12:13] op_sel_hi:[1,0]
	v_pk_mul_f32 v[6:7], v[198:199], s[12:13] op_sel_hi:[1,0]
	v_pk_mul_f32 v[10:11], v[194:195], s[12:13] op_sel_hi:[1,0]
	v_lshlrev_b32_e32 v194, 16, v214
	v_and_b32_e32 v195, 0xffff0000, v214
	v_lshlrev_b32_e32 v196, 16, v215
	v_and_b32_e32 v197, 0xffff0000, v215
	v_lshlrev_b32_e32 v198, 16, v216
	v_and_b32_e32 v199, 0xffff0000, v216
	v_lshlrev_b32_e32 v200, 16, v217
	v_and_b32_e32 v201, 0xffff0000, v217
	v_lshl_add_u64 v[182:183], v[154:155], 0, v[2:3]
	v_lshl_add_u64 v[182:183], v[182:183], 1, s[24:25]
	v_pk_fma_f32 v[142:143], v[142:143], v[14:15], v[194:195]
	v_pk_fma_f32 v[144:145], v[144:145], v[12:13], v[196:197]
	v_pk_fma_f32 v[138:139], v[138:139], v[178:179], v[198:199]
	v_pk_fma_f32 v[140:141], v[140:141], v[16:17], v[200:201]
	v_cvt_pk_bf16_f32 v142, v142, v143
	v_cvt_pk_bf16_f32 v143, v144, v145
	v_cvt_pk_bf16_f32 v144, v138, v139
	v_cvt_pk_bf16_f32 v145, v140, v141
	global_store_dwordx4 v[182:183], v[142:145], off
	v_lshl_add_u64 v[180:181], v[164:165], 0, v[2:3]
	v_lshl_add_u64 v[180:181], v[180:181], 1, s[22:23]
	global_load_dwordx4 v[138:141], v[180:181], off
	s_waitcnt vmcnt(10)
	v_lshlrev_b32_e32 v194, 16, v218
	v_and_b32_e32 v195, 0xffff0000, v218
	v_lshlrev_b32_e32 v196, 16, v219
	v_and_b32_e32 v197, 0xffff0000, v219
	v_lshlrev_b32_e32 v198, 16, v220
	v_and_b32_e32 v199, 0xffff0000, v220
	v_lshlrev_b32_e32 v200, 16, v221
	v_and_b32_e32 v201, 0xffff0000, v221
	v_pk_fma_f32 v[134:135], v[134:135], v[6:7], v[194:195]
	v_pk_fma_f32 v[136:137], v[136:137], v[4:5], v[196:197]
	v_pk_fma_f32 v[130:131], v[130:131], v[10:11], v[198:199]
	v_pk_fma_f32 v[132:133], v[132:133], v[8:9], v[200:201]
	v_cvt_pk_bf16_f32 v134, v134, v135
	v_cvt_pk_bf16_f32 v135, v136, v137
	v_cvt_pk_bf16_f32 v136, v130, v131
	v_cvt_pk_bf16_f32 v137, v132, v133
	global_store_dwordx4 v[182:183], v[134:137], off offset:256
	v_lshl_add_u64 v[180:181], v[164:165], 0, v[2:3]
	v_lshl_add_u64 v[180:181], v[180:181], 1, s[22:23]
	global_load_dwordx4 v[130:133], v[180:181], off offset:256
	s_waitcnt vmcnt(11)
	v_lshlrev_b32_e32 v194, 16, v222
	v_and_b32_e32 v195, 0xffff0000, v222
	v_lshlrev_b32_e32 v196, 16, v223
	v_and_b32_e32 v197, 0xffff0000, v223
	v_lshlrev_b32_e32 v198, 16, v224
	v_and_b32_e32 v199, 0xffff0000, v224
	v_lshlrev_b32_e32 v200, 16, v225
	v_and_b32_e32 v201, 0xffff0000, v225
	v_lshl_add_u64 v[182:183], v[156:157], 0, v[2:3]
	v_lshl_add_u64 v[182:183], v[182:183], 1, s[24:25]
	v_pk_fma_f32 v[126:127], v[126:127], v[14:15], v[194:195]
	v_pk_fma_f32 v[128:129], v[128:129], v[12:13], v[196:197]
	v_pk_fma_f32 v[122:123], v[122:123], v[178:179], v[198:199]
	v_pk_fma_f32 v[124:125], v[124:125], v[16:17], v[200:201]
	v_cvt_pk_bf16_f32 v126, v126, v127
	v_cvt_pk_bf16_f32 v127, v128, v129
	v_cvt_pk_bf16_f32 v128, v122, v123
	v_cvt_pk_bf16_f32 v129, v124, v125
	global_store_dwordx4 v[182:183], v[126:129], off
	v_lshl_add_u64 v[180:181], v[166:167], 0, v[2:3]
	v_lshl_add_u64 v[180:181], v[180:181], 1, s[22:23]
	global_load_dwordx4 v[122:125], v[180:181], off
	s_waitcnt vmcnt(12)
	v_lshlrev_b32_e32 v194, 16, v226
	v_and_b32_e32 v195, 0xffff0000, v226
	v_lshlrev_b32_e32 v196, 16, v227
	v_and_b32_e32 v197, 0xffff0000, v227
	v_lshlrev_b32_e32 v198, 16, v228
	v_and_b32_e32 v199, 0xffff0000, v228
	v_lshlrev_b32_e32 v200, 16, v229
	v_and_b32_e32 v201, 0xffff0000, v229
	v_pk_fma_f32 v[118:119], v[118:119], v[6:7], v[194:195]
	v_pk_fma_f32 v[120:121], v[120:121], v[4:5], v[196:197]
	v_pk_fma_f32 v[114:115], v[114:115], v[10:11], v[198:199]
	v_pk_fma_f32 v[116:117], v[116:117], v[8:9], v[200:201]
	v_cvt_pk_bf16_f32 v118, v118, v119
	v_cvt_pk_bf16_f32 v119, v120, v121
	v_cvt_pk_bf16_f32 v120, v114, v115
	v_cvt_pk_bf16_f32 v121, v116, v117
	global_store_dwordx4 v[182:183], v[118:121], off offset:256
	v_lshl_add_u64 v[180:181], v[166:167], 0, v[2:3]
	v_lshl_add_u64 v[180:181], v[180:181], 1, s[22:23]
	global_load_dwordx4 v[114:117], v[180:181], off offset:256
	s_waitcnt vmcnt(13)
	v_lshlrev_b32_e32 v194, 16, v230
	v_and_b32_e32 v195, 0xffff0000, v230
	v_lshlrev_b32_e32 v196, 16, v231
	v_and_b32_e32 v197, 0xffff0000, v231
	v_lshlrev_b32_e32 v198, 16, v232
	v_and_b32_e32 v199, 0xffff0000, v232
	v_lshlrev_b32_e32 v200, 16, v233
	v_and_b32_e32 v201, 0xffff0000, v233
	v_lshl_add_u64 v[182:183], v[158:159], 0, v[2:3]
	v_lshl_add_u64 v[182:183], v[182:183], 1, s[24:25]
	v_pk_fma_f32 v[110:111], v[110:111], v[14:15], v[194:195]
	v_pk_fma_f32 v[112:113], v[112:113], v[12:13], v[196:197]
	v_pk_fma_f32 v[106:107], v[106:107], v[178:179], v[198:199]
	v_pk_fma_f32 v[108:109], v[108:109], v[16:17], v[200:201]
	v_cvt_pk_bf16_f32 v110, v110, v111
	v_cvt_pk_bf16_f32 v111, v112, v113
	v_cvt_pk_bf16_f32 v112, v106, v107
	v_cvt_pk_bf16_f32 v113, v108, v109
	global_store_dwordx4 v[182:183], v[110:113], off
	v_lshl_add_u64 v[180:181], v[168:169], 0, v[2:3]
	v_lshl_add_u64 v[180:181], v[180:181], 1, s[22:23]
	global_load_dwordx4 v[106:109], v[180:181], off
	s_waitcnt vmcnt(14)
	v_lshlrev_b32_e32 v194, 16, v234
	v_and_b32_e32 v195, 0xffff0000, v234
	v_lshlrev_b32_e32 v196, 16, v235
	v_and_b32_e32 v197, 0xffff0000, v235
	v_lshlrev_b32_e32 v198, 16, v236
	v_and_b32_e32 v199, 0xffff0000, v236
	v_lshlrev_b32_e32 v200, 16, v237
	v_and_b32_e32 v201, 0xffff0000, v237
	v_pk_fma_f32 v[102:103], v[102:103], v[6:7], v[194:195]
	v_pk_fma_f32 v[104:105], v[104:105], v[4:5], v[196:197]
	v_pk_fma_f32 v[98:99], v[98:99], v[10:11], v[198:199]
	v_pk_fma_f32 v[100:101], v[100:101], v[8:9], v[200:201]
	v_cvt_pk_bf16_f32 v102, v102, v103
	v_cvt_pk_bf16_f32 v103, v104, v105
	v_cvt_pk_bf16_f32 v104, v98, v99
	v_cvt_pk_bf16_f32 v105, v100, v101
	global_store_dwordx4 v[182:183], v[102:105], off offset:256
	v_lshl_add_u64 v[180:181], v[168:169], 0, v[2:3]
	v_lshl_add_u64 v[180:181], v[180:181], 1, s[22:23]
	global_load_dwordx4 v[98:101], v[180:181], off offset:256
	s_waitcnt vmcnt(15)
	v_lshlrev_b32_e32 v194, 16, v238
	v_and_b32_e32 v195, 0xffff0000, v238
	v_lshlrev_b32_e32 v196, 16, v239
	v_and_b32_e32 v197, 0xffff0000, v239
	v_lshlrev_b32_e32 v198, 16, v240
	v_and_b32_e32 v199, 0xffff0000, v240
	v_lshlrev_b32_e32 v200, 16, v241
	v_and_b32_e32 v201, 0xffff0000, v241
	v_lshl_add_u64 v[182:183], v[160:161], 0, v[2:3]
	v_lshl_add_u64 v[182:183], v[182:183], 1, s[24:25]
	v_pk_fma_f32 v[94:95], v[94:95], v[14:15], v[194:195]
	v_pk_fma_f32 v[96:97], v[96:97], v[12:13], v[196:197]
	v_pk_fma_f32 v[90:91], v[90:91], v[178:179], v[198:199]
	v_pk_fma_f32 v[92:93], v[92:93], v[16:17], v[200:201]
	v_cvt_pk_bf16_f32 v94, v94, v95
	v_cvt_pk_bf16_f32 v95, v96, v97
	v_cvt_pk_bf16_f32 v96, v90, v91
	v_cvt_pk_bf16_f32 v97, v92, v93
	global_store_dwordx4 v[182:183], v[94:97], off
	s_waitcnt vmcnt(15)
	v_lshlrev_b32_e32 v194, 16, v242
	v_and_b32_e32 v195, 0xffff0000, v242
	v_lshlrev_b32_e32 v196, 16, v243
	v_and_b32_e32 v197, 0xffff0000, v243
	v_lshlrev_b32_e32 v198, 16, v244
	v_and_b32_e32 v199, 0xffff0000, v244
	v_lshlrev_b32_e32 v200, 16, v245
	v_and_b32_e32 v201, 0xffff0000, v245
	v_pk_fma_f32 v[86:87], v[86:87], v[6:7], v[194:195]
	v_pk_fma_f32 v[88:89], v[88:89], v[4:5], v[196:197]
	v_pk_fma_f32 v[82:83], v[82:83], v[10:11], v[198:199]
	v_pk_fma_f32 v[84:85], v[84:85], v[8:9], v[200:201]
	v_cvt_pk_bf16_f32 v86, v86, v87
	v_cvt_pk_bf16_f32 v87, v88, v89
	v_cvt_pk_bf16_f32 v88, v82, v83
	v_cvt_pk_bf16_f32 v89, v84, v85
	global_store_dwordx4 v[182:183], v[86:89], off offset:256
	s_waitcnt vmcnt(15)
	v_lshlrev_b32_e32 v194, 16, v246
	v_and_b32_e32 v195, 0xffff0000, v246
	v_lshlrev_b32_e32 v196, 16, v247
	v_and_b32_e32 v197, 0xffff0000, v247
	v_lshlrev_b32_e32 v198, 16, v248
	v_and_b32_e32 v199, 0xffff0000, v248
	v_lshlrev_b32_e32 v200, 16, v249
	v_and_b32_e32 v201, 0xffff0000, v249
	v_lshl_add_u64 v[182:183], v[162:163], 0, v[2:3]
	v_lshl_add_u64 v[182:183], v[182:183], 1, s[24:25]
	v_pk_fma_f32 v[78:79], v[78:79], v[14:15], v[194:195]
	v_pk_fma_f32 v[80:81], v[80:81], v[12:13], v[196:197]
	v_pk_fma_f32 v[74:75], v[74:75], v[178:179], v[198:199]
	v_pk_fma_f32 v[76:77], v[76:77], v[16:17], v[200:201]
	v_cvt_pk_bf16_f32 v78, v78, v79
	v_cvt_pk_bf16_f32 v79, v80, v81
	v_cvt_pk_bf16_f32 v80, v74, v75
	v_cvt_pk_bf16_f32 v81, v76, v77
	global_store_dwordx4 v[182:183], v[78:81], off
	s_waitcnt vmcnt(15)
	v_lshlrev_b32_e32 v194, 16, v250
	v_and_b32_e32 v195, 0xffff0000, v250
	v_lshlrev_b32_e32 v196, 16, v251
	v_and_b32_e32 v197, 0xffff0000, v251
	v_lshlrev_b32_e32 v198, 16, v252
	v_and_b32_e32 v199, 0xffff0000, v252
	v_lshlrev_b32_e32 v200, 16, v253
	v_and_b32_e32 v201, 0xffff0000, v253
	v_pk_fma_f32 v[70:71], v[70:71], v[6:7], v[194:195]
	v_pk_fma_f32 v[72:73], v[72:73], v[4:5], v[196:197]
	v_pk_fma_f32 v[66:67], v[66:67], v[10:11], v[198:199]
	v_pk_fma_f32 v[68:69], v[68:69], v[8:9], v[200:201]
	v_cvt_pk_bf16_f32 v70, v70, v71
	v_cvt_pk_bf16_f32 v71, v72, v73
	v_cvt_pk_bf16_f32 v72, v66, v67
	v_cvt_pk_bf16_f32 v73, v68, v69
	global_store_dwordx4 v[182:183], v[70:73], off offset:256
	s_waitcnt vmcnt(14)
	v_lshlrev_b32_e32 v194, 16, v138
	v_and_b32_e32 v195, 0xffff0000, v138
	v_lshlrev_b32_e32 v196, 16, v139
	v_and_b32_e32 v197, 0xffff0000, v139
	v_lshlrev_b32_e32 v198, 16, v140
	v_and_b32_e32 v199, 0xffff0000, v140
	v_lshlrev_b32_e32 v200, 16, v141
	v_and_b32_e32 v201, 0xffff0000, v141
	v_lshl_add_u64 v[182:183], v[164:165], 0, v[2:3]
	v_lshl_add_u64 v[182:183], v[182:183], 1, s[24:25]
	v_pk_fma_f32 v[62:63], v[62:63], v[14:15], v[194:195]
	v_pk_fma_f32 v[64:65], v[64:65], v[12:13], v[196:197]
	v_pk_fma_f32 v[58:59], v[58:59], v[178:179], v[198:199]
	v_pk_fma_f32 v[60:61], v[60:61], v[16:17], v[200:201]
	v_cvt_pk_bf16_f32 v62, v62, v63
	v_cvt_pk_bf16_f32 v63, v64, v65
	v_cvt_pk_bf16_f32 v64, v58, v59
	v_cvt_pk_bf16_f32 v65, v60, v61
	global_store_dwordx4 v[182:183], v[62:65], off
	s_waitcnt vmcnt(13)
	v_lshlrev_b32_e32 v194, 16, v130
	v_and_b32_e32 v195, 0xffff0000, v130
	v_lshlrev_b32_e32 v196, 16, v131
	v_and_b32_e32 v197, 0xffff0000, v131
	v_lshlrev_b32_e32 v198, 16, v132
	v_and_b32_e32 v199, 0xffff0000, v132
	v_lshlrev_b32_e32 v200, 16, v133
	v_and_b32_e32 v201, 0xffff0000, v133
	v_pk_fma_f32 v[54:55], v[54:55], v[6:7], v[194:195]
	v_pk_fma_f32 v[56:57], v[56:57], v[4:5], v[196:197]
	v_pk_fma_f32 v[50:51], v[50:51], v[10:11], v[198:199]
	v_pk_fma_f32 v[52:53], v[52:53], v[8:9], v[200:201]
	v_cvt_pk_bf16_f32 v54, v54, v55
	v_cvt_pk_bf16_f32 v55, v56, v57
	v_cvt_pk_bf16_f32 v56, v50, v51
	v_cvt_pk_bf16_f32 v57, v52, v53
	global_store_dwordx4 v[182:183], v[54:57], off offset:256
	s_waitcnt vmcnt(12)
	v_lshlrev_b32_e32 v194, 16, v122
	v_and_b32_e32 v195, 0xffff0000, v122
	v_lshlrev_b32_e32 v196, 16, v123
	v_and_b32_e32 v197, 0xffff0000, v123
	v_lshlrev_b32_e32 v198, 16, v124
	v_and_b32_e32 v199, 0xffff0000, v124
	v_lshlrev_b32_e32 v200, 16, v125
	v_and_b32_e32 v201, 0xffff0000, v125
	v_lshl_add_u64 v[182:183], v[166:167], 0, v[2:3]
	v_lshl_add_u64 v[182:183], v[182:183], 1, s[24:25]
	v_pk_fma_f32 v[46:47], v[46:47], v[14:15], v[194:195]
	v_pk_fma_f32 v[48:49], v[48:49], v[12:13], v[196:197]
	v_pk_fma_f32 v[42:43], v[42:43], v[178:179], v[198:199]
	v_pk_fma_f32 v[44:45], v[44:45], v[16:17], v[200:201]
	v_cvt_pk_bf16_f32 v46, v46, v47
	v_cvt_pk_bf16_f32 v47, v48, v49
	v_cvt_pk_bf16_f32 v48, v42, v43
	v_cvt_pk_bf16_f32 v49, v44, v45
	global_store_dwordx4 v[182:183], v[46:49], off
	s_waitcnt vmcnt(11)
	v_lshlrev_b32_e32 v194, 16, v114
	v_and_b32_e32 v195, 0xffff0000, v114
	v_lshlrev_b32_e32 v196, 16, v115
	v_and_b32_e32 v197, 0xffff0000, v115
	v_lshlrev_b32_e32 v198, 16, v116
	v_and_b32_e32 v199, 0xffff0000, v116
	v_lshlrev_b32_e32 v200, 16, v117
	v_and_b32_e32 v201, 0xffff0000, v117
	v_pk_fma_f32 v[38:39], v[38:39], v[6:7], v[194:195]
	v_pk_fma_f32 v[40:41], v[40:41], v[4:5], v[196:197]
	v_pk_fma_f32 v[34:35], v[34:35], v[10:11], v[198:199]
	v_pk_fma_f32 v[36:37], v[36:37], v[8:9], v[200:201]
	v_cvt_pk_bf16_f32 v38, v38, v39
	v_cvt_pk_bf16_f32 v39, v40, v41
	v_cvt_pk_bf16_f32 v40, v34, v35
	v_cvt_pk_bf16_f32 v41, v36, v37
	global_store_dwordx4 v[182:183], v[38:41], off offset:256
	s_waitcnt vmcnt(10)
	v_lshlrev_b32_e32 v194, 16, v106
	v_and_b32_e32 v195, 0xffff0000, v106
	v_lshlrev_b32_e32 v196, 16, v107
	v_and_b32_e32 v197, 0xffff0000, v107
	v_lshlrev_b32_e32 v198, 16, v108
	v_and_b32_e32 v199, 0xffff0000, v108
	v_lshlrev_b32_e32 v200, 16, v109
	v_and_b32_e32 v201, 0xffff0000, v109
	v_lshl_add_u64 v[182:183], v[168:169], 0, v[2:3]
	v_lshl_add_u64 v[182:183], v[182:183], 1, s[24:25]
	v_pk_fma_f32 v[30:31], v[30:31], v[14:15], v[194:195]
	v_pk_fma_f32 v[32:33], v[32:33], v[12:13], v[196:197]
	v_pk_fma_f32 v[26:27], v[26:27], v[178:179], v[198:199]
	v_pk_fma_f32 v[28:29], v[28:29], v[16:17], v[200:201]
	v_cvt_pk_bf16_f32 v30, v30, v31
	v_cvt_pk_bf16_f32 v31, v32, v33
	v_cvt_pk_bf16_f32 v32, v26, v27
	v_cvt_pk_bf16_f32 v33, v28, v29
	global_store_dwordx4 v[182:183], v[30:33], off
	s_waitcnt vmcnt(9)
	v_lshlrev_b32_e32 v194, 16, v98
	v_and_b32_e32 v195, 0xffff0000, v98
	v_lshlrev_b32_e32 v196, 16, v99
	v_and_b32_e32 v197, 0xffff0000, v99
	v_lshlrev_b32_e32 v198, 16, v100
	v_and_b32_e32 v199, 0xffff0000, v100
	v_lshlrev_b32_e32 v200, 16, v101
	v_and_b32_e32 v201, 0xffff0000, v101
	v_pk_fma_f32 v[22:23], v[22:23], v[6:7], v[194:195]
	v_pk_fma_f32 v[24:25], v[24:25], v[4:5], v[196:197]
	v_pk_fma_f32 v[18:19], v[18:19], v[10:11], v[198:199]
	v_pk_fma_f32 v[20:21], v[20:21], v[8:9], v[200:201]
	v_cvt_pk_bf16_f32 v22, v22, v23
	v_cvt_pk_bf16_f32 v23, v24, v25
	v_cvt_pk_bf16_f32 v24, v18, v19
	v_cvt_pk_bf16_f32 v25, v20, v21
	global_store_dwordx4 v[182:183], v[22:25], off offset:256
	s_mov_b32 s22, s16
	s_mov_b64 s[24:25], s[18:19]
	s_and_b64 vcc, exec, s[0:1]
	s_cbranch_vccnz .LBB0_1235
